# priority alternation with waves 4-7 prioritised for 40 of every 64 fragments (waves 0-3 for 24)
# speedup vs baseline: 1.0062x; 1.0033x over previous
.Lattn_pbx0:
	s_waitcnt lgkmcnt(6)
	v_mfma_f32_16x16x32_bf16 v[64:67], v[160:163], v[96:99], 0
	v_exp_f32_e32 v88, v88
	v_mfma_f32_16x16x32_bf16 v[68:71], v[160:163], v[112:115], 0
	v_exp_f32_e32 v92, v92
	ds_read_b128 v[234:237], v209 offset:6144
	s_add_u32 s16, s22, s10
	s_addc_u32 s17, s23, s11
	s_add_u32 s15, s22, s12
	s_addc_u32 s14, s23, s13
	s_add_u32 s8, s16, 0x3bc00200
	s_addc_u32 s9, s17, 0
	s_add_u32 s6, s15, 0x23a50000
	s_addc_u32 s7, s14, 0
	s_waitcnt lgkmcnt(6)
	v_mfma_f32_16x16x32_bf16 v[0:3], v[164:167], v[216:219], v[0:3]
	v_cvt_pk_bf16_f32 v242, v80, v81
	v_mfma_f32_16x16x32_bf16 v[4:7], v[164:167], v[238:241], v[4:7]
	v_exp_f32_e32 v89, v89
	ds_read_b128 v[160:163], v201 offset:20480
	s_waitcnt vmcnt(4)
	ds_write_b128 v225, v[152:155] offset:49152
	s_waitcnt lgkmcnt(7)
	v_mfma_f32_16x16x32_bf16 v[68:71], v[168:171], v[116:119], v[68:71]
	v_exp_f32_e32 v93, v93
	v_mfma_f32_16x16x32_bf16 v[64:67], v[168:171], v[100:103], v[64:67]
	v_cvt_pk_bf16_f32 v243, v82, v83
	ds_read_b128 v[164:167], v209 offset:8192
	ds_write_b128 v226, v[156:159] offset:49152
	s_waitcnt lgkmcnt(8)
	v_mfma_f32_16x16x32_bf16 v[12:15], v[172:175], v[238:241], v[12:15]
	v_exp_f32_e32 v90, v90
	v_mfma_f32_16x16x32_bf16 v[8:11], v[172:175], v[216:219], v[8:11]
	v_exp_f32_e32 v94, v94
	ds_read_b128 v[168:171], v202 offset:20480
	ds_write_b64 v227, v[132:133] offset:32768
	s_waitcnt lgkmcnt(9)
	v_mfma_f32_16x16x32_bf16 v[64:67], v[176:179], v[104:107], v[64:67]
	v_cvt_pk_bf16_f32 v204, v84, v85
	v_mfma_f32_16x16x32_bf16 v[68:71], v[176:179], v[120:123], v[68:71]
	v_exp_f32_e32 v91, v91
	ds_read_b128 v[172:175], v209 offset:10240
	ds_write_b64 v228, v[134:135] offset:32768
	s_waitcnt lgkmcnt(10)
	v_mfma_f32_16x16x32_bf16 v[16:19], v[180:183], v[216:219], v[16:19]
	v_exp_f32_e32 v95, v95
	v_mfma_f32_16x16x32_bf16 v[20:23], v[180:183], v[238:241], v[20:23]
	v_cvt_pk_bf16_f32 v205, v86, v87
	v_add_f32_e32 v220, v220, v88
	ds_read_b128 v[176:179], v203 offset:20480
	ds_write_b64 v229, v[128:129] offset:32768
	s_waitcnt lgkmcnt(11)
	v_mfma_f32_16x16x32_bf16 v[68:71], v[230:233], v[124:127], v[68:71]
	v_add_f32_e32 v221, v221, v92
	v_add_f32_e32 v220, v220, v89
	v_mfma_f32_16x16x32_bf16 v[64:67], v[230:233], v[108:111], v[64:67]
	v_add_f32_e32 v221, v221, v93
	v_cvt_pk_bf16_f32 v244, v88, v89
	ds_read_b128 v[180:183], v209 offset:12288
	ds_write_b64 v184, v[130:131] offset:32768
	s_waitcnt lgkmcnt(12)
	v_mfma_f32_16x16x32_bf16 v[28:31], v[234:237], v[238:241], v[28:31]
	v_cvt_pk_bf16_f32 v245, v90, v91
	v_cvt_pk_bf16_f32 v206, v92, v93
	v_mfma_f32_16x16x32_bf16 v[24:27], v[234:237], v[216:219], v[24:27]
	v_cvt_pk_bf16_f32 v207, v94, v95
	ds_read_b128 v[230:233], v246 offset:20480
	global_load_dwordx4 v[132:135], v198, s[8:9]
	s_waitcnt lgkmcnt(12)
	v_mfma_f32_16x16x32_bf16 v[72:75], v[160:163], v[96:99], 0
	v_add_f32_e32 v220, v220, v90
	v_add_f32_e32 v221, v221, v94
	v_mfma_f32_16x16x32_bf16 v[76:79], v[160:163], v[112:115], 0
	v_add_f32_e32 v220, v220, v91
	v_add_f32_e32 v221, v221, v95
	ds_read_b128 v[234:237], v209 offset:14336
	global_load_dwordx4 v[128:131], v199, s[8:9]
	s_waitcnt lgkmcnt(11)
	v_mfma_f32_16x16x32_bf16 v[32:35], v[164:167], v[216:219], v[32:35]
	v_add_f32_e32 v194, v194, v220
	v_add_f32_e32 v195, v195, v221
	v_mfma_f32_16x16x32_bf16 v[36:39], v[164:167], v[238:241], v[36:39]
	v_exp_f32_e32 v64, v64
	ds_read_b128 v[160:163], v201 offset:24576
	global_load_dwordx4 v[152:155], v196, s[6:7]
	s_waitcnt lgkmcnt(10)
	v_mfma_f32_16x16x32_bf16 v[76:79], v[168:171], v[116:119], v[76:79]
	v_exp_f32_e32 v68, v68
	v_mfma_f32_16x16x32_bf16 v[72:75], v[168:171], v[100:103], v[72:75]
	v_exp_f32_e32 v65, v65
	ds_read_b128 v[164:167], v210 offset:0
	global_load_dwordx4 v[156:159], v197, s[6:7]
	s_waitcnt lgkmcnt(9)
	v_mfma_f32_16x16x32_bf16 v[44:47], v[172:175], v[238:241], v[44:47]
	v_exp_f32_e32 v69, v69
	v_mfma_f32_16x16x32_bf16 v[40:43], v[172:175], v[216:219], v[40:43]
	v_exp_f32_e32 v66, v66
	ds_read_b128 v[168:171], v202 offset:24576
	s_waitcnt lgkmcnt(8)
	v_mfma_f32_16x16x32_bf16 v[72:75], v[176:179], v[104:107], v[72:75]
	v_exp_f32_e32 v70, v70
	v_mfma_f32_16x16x32_bf16 v[76:79], v[176:179], v[120:123], v[76:79]
	v_exp_f32_e32 v67, v67
	ds_read_b128 v[172:175], v210 offset:2048
	s_waitcnt lgkmcnt(7)
	v_mfma_f32_16x16x32_bf16 v[48:51], v[180:183], v[216:219], v[48:51]
	v_exp_f32_e32 v71, v71
	v_mfma_f32_16x16x32_bf16 v[52:55], v[180:183], v[238:241], v[52:55]
	v_add_f32_e32 v220, v64, v65
	ds_read_b128 v[176:179], v203 offset:24576
	s_waitcnt lgkmcnt(6)
	v_mfma_f32_16x16x32_bf16 v[76:79], v[230:233], v[124:127], v[76:79]
	v_add_f32_e32 v221, v68, v69
	v_mfma_f32_16x16x32_bf16 v[72:75], v[230:233], v[108:111], v[72:75]
	v_add_f32_e32 v220, v220, v66
	ds_read_b128 v[180:183], v210 offset:4096
	s_waitcnt lgkmcnt(6)
	v_mfma_f32_16x16x32_bf16 v[60:63], v[234:237], v[238:241], v[60:63]
	v_add_f32_e32 v221, v221, v70
	v_add_f32_e32 v220, v220, v67
	v_mfma_f32_16x16x32_bf16 v[56:59], v[234:237], v[216:219], v[56:59]
	v_add_f32_e32 v221, v221, v71
	ds_read_b128 v[230:233], v246 offset:24576
	s_waitcnt lgkmcnt(6)
	v_mfma_f32_16x16x32_bf16 v[80:83], v[160:163], v[96:99], 0
	v_exp_f32_e32 v72, v72
	v_mfma_f32_16x16x32_bf16 v[84:87], v[160:163], v[112:115], 0
	v_exp_f32_e32 v76, v76
	ds_read_b128 v[234:237], v210 offset:6144
	s_waitcnt lgkmcnt(6)
	v_mfma_f32_16x16x32_bf16 v[0:3], v[164:167], v[242:245], v[0:3]
	v_exp_f32_e32 v73, v73
	v_mfma_f32_16x16x32_bf16 v[4:7], v[164:167], v[204:207], v[4:7]
	v_exp_f32_e32 v77, v77
	ds_read_b128 v[160:163], v201 offset:28672
	s_waitcnt lgkmcnt(6)
	v_mfma_f32_16x16x32_bf16 v[84:87], v[168:171], v[116:119], v[84:87]
	v_exp_f32_e32 v74, v74
	v_mfma_f32_16x16x32_bf16 v[80:83], v[168:171], v[100:103], v[80:83]
	v_exp_f32_e32 v78, v78
	ds_read_b128 v[164:167], v210 offset:8192
	s_waitcnt lgkmcnt(6)
	v_mfma_f32_16x16x32_bf16 v[12:15], v[172:175], v[204:207], v[12:15]
	v_exp_f32_e32 v75, v75
	v_mfma_f32_16x16x32_bf16 v[8:11], v[172:175], v[242:245], v[8:11]
	v_exp_f32_e32 v79, v79
	ds_read_b128 v[168:171], v202 offset:28672
	s_waitcnt lgkmcnt(6)
	v_mfma_f32_16x16x32_bf16 v[80:83], v[176:179], v[104:107], v[80:83]
	v_add_f32_e32 v220, v220, v72
	v_add_f32_e32 v221, v221, v76
	v_mfma_f32_16x16x32_bf16 v[84:87], v[176:179], v[120:123], v[84:87]
	v_add_f32_e32 v220, v220, v73
	ds_read_b128 v[172:175], v210 offset:10240
	s_waitcnt lgkmcnt(6)
	v_mfma_f32_16x16x32_bf16 v[16:19], v[180:183], v[242:245], v[16:19]
	v_add_f32_e32 v221, v221, v77
	v_add_f32_e32 v220, v220, v74
	v_mfma_f32_16x16x32_bf16 v[20:23], v[180:183], v[204:207], v[20:23]
	v_add_f32_e32 v221, v221, v78
	ds_read_b128 v[176:179], v203 offset:28672
	s_waitcnt lgkmcnt(6)
	v_mfma_f32_16x16x32_bf16 v[84:87], v[230:233], v[124:127], v[84:87]
	v_add_f32_e32 v220, v220, v75
	v_add_f32_e32 v221, v221, v79
	v_mfma_f32_16x16x32_bf16 v[80:83], v[230:233], v[108:111], v[80:83]
	v_cvt_pk_bf16_f32 v216, v64, v65
	ds_read_b128 v[180:183], v210 offset:12288
	s_waitcnt lgkmcnt(6)
	v_mfma_f32_16x16x32_bf16 v[28:31], v[234:237], v[204:207], v[28:31]
	v_cvt_pk_bf16_f32 v217, v66, v67
	v_cvt_pk_bf16_f32 v238, v68, v69
	v_mfma_f32_16x16x32_bf16 v[24:27], v[234:237], v[242:245], v[24:27]
	v_cvt_pk_bf16_f32 v239, v70, v71
	ds_read_b128 v[230:233], v246 offset:28672
	s_waitcnt lgkmcnt(6)
	v_mfma_f32_16x16x32_bf16 v[88:91], v[160:163], v[96:99], 0
	v_exp_f32_e32 v80, v80
	v_mfma_f32_16x16x32_bf16 v[92:95], v[160:163], v[112:115], 0
	v_exp_f32_e32 v84, v84
	ds_read_b128 v[234:237], v210 offset:14336
	s_waitcnt lgkmcnt(6)
	v_mfma_f32_16x16x32_bf16 v[32:35], v[164:167], v[242:245], v[32:35]
	v_exp_f32_e32 v81, v81
	v_mfma_f32_16x16x32_bf16 v[36:39], v[164:167], v[204:207], v[36:39]
	v_exp_f32_e32 v85, v85
	ds_read_b128 v[160:163], v201 offset:32768
	s_waitcnt lgkmcnt(6)
	v_mfma_f32_16x16x32_bf16 v[92:95], v[168:171], v[116:119], v[92:95]
	v_exp_f32_e32 v82, v82
	v_mfma_f32_16x16x32_bf16 v[88:91], v[168:171], v[100:103], v[88:91]
	v_exp_f32_e32 v86, v86
	ds_read_b128 v[164:167], v209 offset:16384
	s_waitcnt lgkmcnt(6)
	v_mfma_f32_16x16x32_bf16 v[44:47], v[172:175], v[204:207], v[44:47]
	v_exp_f32_e32 v83, v83
	v_mfma_f32_16x16x32_bf16 v[40:43], v[172:175], v[242:245], v[40:43]
	v_exp_f32_e32 v87, v87
	ds_read_b128 v[168:171], v202 offset:32768
	s_waitcnt lgkmcnt(6)
	v_mfma_f32_16x16x32_bf16 v[88:91], v[176:179], v[104:107], v[88:91]
	v_add_f32_e32 v220, v220, v80
	v_add_f32_e32 v221, v221, v84
	v_mfma_f32_16x16x32_bf16 v[92:95], v[176:179], v[120:123], v[92:95]
	v_add_f32_e32 v220, v220, v81
	ds_read_b128 v[172:175], v209 offset:18432
	s_waitcnt lgkmcnt(6)
	v_mfma_f32_16x16x32_bf16 v[48:51], v[180:183], v[242:245], v[48:51]
	v_add_f32_e32 v221, v221, v85
	v_add_f32_e32 v220, v220, v82
	v_mfma_f32_16x16x32_bf16 v[52:55], v[180:183], v[204:207], v[52:55]
	v_add_f32_e32 v221, v221, v86
	ds_read_b128 v[176:179], v203 offset:32768
	s_waitcnt lgkmcnt(6)
	v_mfma_f32_16x16x32_bf16 v[92:95], v[230:233], v[124:127], v[92:95]
	v_add_f32_e32 v220, v220, v83
	v_add_f32_e32 v221, v221, v87
	v_mfma_f32_16x16x32_bf16 v[88:91], v[230:233], v[108:111], v[88:91]
	v_cvt_pk_bf16_f32 v218, v72, v73
	ds_read_b128 v[180:183], v209 offset:20480
	s_waitcnt lgkmcnt(6)
	v_mfma_f32_16x16x32_bf16 v[60:63], v[234:237], v[204:207], v[60:63]
	v_cvt_pk_bf16_f32 v219, v74, v75
	v_cvt_pk_bf16_f32 v240, v76, v77
	v_mfma_f32_16x16x32_bf16 v[56:59], v[234:237], v[242:245], v[56:59]
	v_cvt_pk_bf16_f32 v241, v78, v79
	ds_read_b128 v[230:233], v246 offset:32768
	s_waitcnt lgkmcnt(6)
	v_mfma_f32_16x16x32_bf16 v[64:67], v[160:163], v[96:99], 0
	v_exp_f32_e32 v88, v88
	v_mfma_f32_16x16x32_bf16 v[68:71], v[160:163], v[112:115], 0
	v_exp_f32_e32 v92, v92
	ds_read_b128 v[234:237], v209 offset:22528
	s_add_u32 s8, s16, 0x3bc00280
	s_addc_u32 s9, s17, 0
	s_add_u32 s6, s15, 0x23a60000
	s_addc_u32 s7, s14, 0
	s_waitcnt lgkmcnt(6)
	v_mfma_f32_16x16x32_bf16 v[0:3], v[164:167], v[216:219], v[0:3]
	v_cvt_pk_bf16_f32 v242, v80, v81
	v_mfma_f32_16x16x32_bf16 v[4:7], v[164:167], v[238:241], v[4:7]
	v_exp_f32_e32 v89, v89
	ds_read_b128 v[160:163], v201 offset:36864
	s_waitcnt vmcnt(4)
	ds_write_b128 v225, v[136:139] offset:0
	s_waitcnt lgkmcnt(7)
	v_mfma_f32_16x16x32_bf16 v[68:71], v[168:171], v[116:119], v[68:71]
	v_exp_f32_e32 v93, v93
	v_mfma_f32_16x16x32_bf16 v[64:67], v[168:171], v[100:103], v[64:67]
	v_cvt_pk_bf16_f32 v243, v82, v83
	ds_read_b128 v[164:167], v209 offset:24576
	ds_write_b128 v226, v[140:143] offset:0
	s_waitcnt lgkmcnt(8)
	v_mfma_f32_16x16x32_bf16 v[12:15], v[172:175], v[238:241], v[12:15]
	v_exp_f32_e32 v90, v90
	v_mfma_f32_16x16x32_bf16 v[8:11], v[172:175], v[216:219], v[8:11]
	v_exp_f32_e32 v94, v94
	ds_read_b128 v[168:171], v202 offset:36864
	ds_write_b64 v227, v[148:149] offset:49152
	s_waitcnt lgkmcnt(9)
	v_mfma_f32_16x16x32_bf16 v[64:67], v[176:179], v[104:107], v[64:67]
	v_cvt_pk_bf16_f32 v204, v84, v85
	v_mfma_f32_16x16x32_bf16 v[68:71], v[176:179], v[120:123], v[68:71]
	v_exp_f32_e32 v91, v91
	ds_read_b128 v[172:175], v209 offset:26624
	ds_write_b64 v228, v[150:151] offset:49152
	s_waitcnt lgkmcnt(10)
	v_mfma_f32_16x16x32_bf16 v[16:19], v[180:183], v[216:219], v[16:19]
	v_exp_f32_e32 v95, v95
	v_mfma_f32_16x16x32_bf16 v[20:23], v[180:183], v[238:241], v[20:23]
	v_cvt_pk_bf16_f32 v205, v86, v87
	v_add_f32_e32 v220, v220, v88
	ds_read_b128 v[176:179], v203 offset:36864
	ds_write_b64 v229, v[144:145] offset:49152
	s_waitcnt lgkmcnt(11)
	v_mfma_f32_16x16x32_bf16 v[68:71], v[230:233], v[124:127], v[68:71]
	v_add_f32_e32 v221, v221, v92
	v_add_f32_e32 v220, v220, v89
	v_mfma_f32_16x16x32_bf16 v[64:67], v[230:233], v[108:111], v[64:67]
	v_add_f32_e32 v221, v221, v93
	v_cvt_pk_bf16_f32 v244, v88, v89
	ds_read_b128 v[180:183], v209 offset:28672
	ds_write_b64 v184, v[146:147] offset:49152
	s_waitcnt lgkmcnt(12)
	v_mfma_f32_16x16x32_bf16 v[28:31], v[234:237], v[238:241], v[28:31]
	v_cvt_pk_bf16_f32 v245, v90, v91
	v_cvt_pk_bf16_f32 v206, v92, v93
	v_mfma_f32_16x16x32_bf16 v[24:27], v[234:237], v[216:219], v[24:27]
	v_cvt_pk_bf16_f32 v207, v94, v95
	ds_read_b128 v[230:233], v246 offset:36864
	global_load_dwordx4 v[148:151], v198, s[8:9]
	s_cmp_eq_u32 s100, 1
	s_cbranch_scc1 .Lattn_pax40
	s_setprio 1
	s_branch .Lattn_pbx40

.Lattn_pbx40:
	s_waitcnt lgkmcnt(12)
	v_mfma_f32_16x16x32_bf16 v[72:75], v[160:163], v[96:99], 0
	v_add_f32_e32 v220, v220, v90
	v_add_f32_e32 v221, v221, v94
	v_mfma_f32_16x16x32_bf16 v[76:79], v[160:163], v[112:115], 0
	v_add_f32_e32 v220, v220, v91
	v_add_f32_e32 v221, v221, v95
	ds_read_b128 v[234:237], v209 offset:30720
	global_load_dwordx4 v[144:147], v199, s[8:9]
	s_waitcnt lgkmcnt(11)
	v_mfma_f32_16x16x32_bf16 v[32:35], v[164:167], v[216:219], v[32:35]
	v_add_f32_e32 v194, v194, v220
	v_add_f32_e32 v195, v195, v221
	v_mfma_f32_16x16x32_bf16 v[36:39], v[164:167], v[238:241], v[36:39]
	v_exp_f32_e32 v64, v64
	ds_read_b128 v[160:163], v201 offset:40960
	global_load_dwordx4 v[136:139], v196, s[6:7]
	s_waitcnt lgkmcnt(10)
	v_mfma_f32_16x16x32_bf16 v[76:79], v[168:171], v[116:119], v[76:79]
	v_exp_f32_e32 v68, v68
	v_mfma_f32_16x16x32_bf16 v[72:75], v[168:171], v[100:103], v[72:75]
	v_exp_f32_e32 v65, v65
	ds_read_b128 v[164:167], v210 offset:16384
	global_load_dwordx4 v[140:143], v197, s[6:7]
	s_waitcnt lgkmcnt(9)
	v_mfma_f32_16x16x32_bf16 v[44:47], v[172:175], v[238:241], v[44:47]
	v_exp_f32_e32 v69, v69
	v_mfma_f32_16x16x32_bf16 v[40:43], v[172:175], v[216:219], v[40:43]
	v_exp_f32_e32 v66, v66
	ds_read_b128 v[168:171], v202 offset:40960
	s_waitcnt lgkmcnt(8)
	v_mfma_f32_16x16x32_bf16 v[72:75], v[176:179], v[104:107], v[72:75]
	v_exp_f32_e32 v70, v70
	v_mfma_f32_16x16x32_bf16 v[76:79], v[176:179], v[120:123], v[76:79]
	v_exp_f32_e32 v67, v67
	ds_read_b128 v[172:175], v210 offset:18432
	s_waitcnt lgkmcnt(7)
	v_mfma_f32_16x16x32_bf16 v[48:51], v[180:183], v[216:219], v[48:51]
	v_exp_f32_e32 v71, v71
	v_mfma_f32_16x16x32_bf16 v[52:55], v[180:183], v[238:241], v[52:55]
	v_add_f32_e32 v220, v64, v65
	ds_read_b128 v[176:179], v203 offset:40960
	s_waitcnt lgkmcnt(6)
	v_mfma_f32_16x16x32_bf16 v[76:79], v[230:233], v[124:127], v[76:79]
	v_add_f32_e32 v221, v68, v69
	v_mfma_f32_16x16x32_bf16 v[72:75], v[230:233], v[108:111], v[72:75]
	v_add_f32_e32 v220, v220, v66
	ds_read_b128 v[180:183], v210 offset:20480
	s_waitcnt lgkmcnt(6)
	v_mfma_f32_16x16x32_bf16 v[60:63], v[234:237], v[238:241], v[60:63]
	v_add_f32_e32 v221, v221, v70
	v_add_f32_e32 v220, v220, v67
	v_mfma_f32_16x16x32_bf16 v[56:59], v[234:237], v[216:219], v[56:59]
	v_add_f32_e32 v221, v221, v71
	ds_read_b128 v[230:233], v246 offset:40960
	s_waitcnt lgkmcnt(6)
	v_mfma_f32_16x16x32_bf16 v[80:83], v[160:163], v[96:99], 0
	v_exp_f32_e32 v72, v72
	v_mfma_f32_16x16x32_bf16 v[84:87], v[160:163], v[112:115], 0
	v_exp_f32_e32 v76, v76
	ds_read_b128 v[234:237], v210 offset:22528
	s_waitcnt lgkmcnt(6)
	v_mfma_f32_16x16x32_bf16 v[0:3], v[164:167], v[242:245], v[0:3]
	v_exp_f32_e32 v73, v73
	v_mfma_f32_16x16x32_bf16 v[4:7], v[164:167], v[204:207], v[4:7]
	v_exp_f32_e32 v77, v77
	ds_read_b128 v[160:163], v201 offset:45056
	s_waitcnt lgkmcnt(6)
	v_mfma_f32_16x16x32_bf16 v[84:87], v[168:171], v[116:119], v[84:87]
	v_exp_f32_e32 v74, v74
	v_mfma_f32_16x16x32_bf16 v[80:83], v[168:171], v[100:103], v[80:83]
	v_exp_f32_e32 v78, v78
	ds_read_b128 v[164:167], v210 offset:24576
	s_waitcnt lgkmcnt(6)
	v_mfma_f32_16x16x32_bf16 v[12:15], v[172:175], v[204:207], v[12:15]
	v_exp_f32_e32 v75, v75
	v_mfma_f32_16x16x32_bf16 v[8:11], v[172:175], v[242:245], v[8:11]
	v_exp_f32_e32 v79, v79
	ds_read_b128 v[168:171], v202 offset:45056
	s_waitcnt lgkmcnt(6)
	v_mfma_f32_16x16x32_bf16 v[80:83], v[176:179], v[104:107], v[80:83]
	v_add_f32_e32 v220, v220, v72
	v_add_f32_e32 v221, v221, v76
	v_mfma_f32_16x16x32_bf16 v[84:87], v[176:179], v[120:123], v[84:87]
	v_add_f32_e32 v220, v220, v73
	ds_read_b128 v[172:175], v210 offset:26624
	s_waitcnt lgkmcnt(6)
	v_mfma_f32_16x16x32_bf16 v[16:19], v[180:183], v[242:245], v[16:19]
	v_add_f32_e32 v221, v221, v77
	v_add_f32_e32 v220, v220, v74
	v_mfma_f32_16x16x32_bf16 v[20:23], v[180:183], v[204:207], v[20:23]
	v_add_f32_e32 v221, v221, v78
	ds_read_b128 v[176:179], v203 offset:45056
	s_waitcnt lgkmcnt(6)
	v_mfma_f32_16x16x32_bf16 v[84:87], v[230:233], v[124:127], v[84:87]
	v_add_f32_e32 v220, v220, v75
	v_add_f32_e32 v221, v221, v79
	v_mfma_f32_16x16x32_bf16 v[80:83], v[230:233], v[108:111], v[80:83]
	v_cvt_pk_bf16_f32 v216, v64, v65
	ds_read_b128 v[180:183], v210 offset:28672
	s_waitcnt lgkmcnt(6)
	v_mfma_f32_16x16x32_bf16 v[28:31], v[234:237], v[204:207], v[28:31]
	v_cvt_pk_bf16_f32 v217, v66, v67
	v_cvt_pk_bf16_f32 v238, v68, v69
	v_mfma_f32_16x16x32_bf16 v[24:27], v[234:237], v[242:245], v[24:27]
	v_cvt_pk_bf16_f32 v239, v70, v71
	ds_read_b128 v[230:233], v246 offset:45056
	s_waitcnt lgkmcnt(6)
	v_mfma_f32_16x16x32_bf16 v[88:91], v[160:163], v[96:99], 0
	v_exp_f32_e32 v80, v80
	v_mfma_f32_16x16x32_bf16 v[92:95], v[160:163], v[112:115], 0
	v_exp_f32_e32 v84, v84
	ds_read_b128 v[234:237], v210 offset:30720
	s_waitcnt lgkmcnt(6)
	v_mfma_f32_16x16x32_bf16 v[32:35], v[164:167], v[242:245], v[32:35]
	v_exp_f32_e32 v81, v81
	v_mfma_f32_16x16x32_bf16 v[36:39], v[164:167], v[204:207], v[36:39]
	v_exp_f32_e32 v85, v85
	s_waitcnt lgkmcnt(5)
	v_mfma_f32_16x16x32_bf16 v[92:95], v[168:171], v[116:119], v[92:95]
	v_exp_f32_e32 v82, v82
	v_mfma_f32_16x16x32_bf16 v[88:91], v[168:171], v[100:103], v[88:91]
	v_exp_f32_e32 v86, v86
	s_waitcnt lgkmcnt(4)
	v_mfma_f32_16x16x32_bf16 v[44:47], v[172:175], v[204:207], v[44:47]
	v_exp_f32_e32 v83, v83
	v_mfma_f32_16x16x32_bf16 v[40:43], v[172:175], v[242:245], v[40:43]
	v_exp_f32_e32 v87, v87
	s_waitcnt lgkmcnt(3)
	v_mfma_f32_16x16x32_bf16 v[88:91], v[176:179], v[104:107], v[88:91]
	v_add_f32_e32 v220, v220, v80
	v_add_f32_e32 v221, v221, v84
	v_mfma_f32_16x16x32_bf16 v[92:95], v[176:179], v[120:123], v[92:95]
	v_add_f32_e32 v220, v220, v81
	s_waitcnt lgkmcnt(0)
	s_barrier
	ds_read_b128 v[160:163], v201 offset:49152
	ds_read_b128 v[164:167], v209 offset:32768
	ds_read_b128 v[168:171], v202 offset:49152
	ds_read_b128 v[172:175], v209 offset:34816
	v_mfma_f32_16x16x32_bf16 v[48:51], v[180:183], v[242:245], v[48:51]
	v_add_f32_e32 v221, v221, v85
	v_add_f32_e32 v220, v220, v82
	v_mfma_f32_16x16x32_bf16 v[52:55], v[180:183], v[204:207], v[52:55]
	v_add_f32_e32 v221, v221, v86
	ds_read_b128 v[176:179], v203 offset:49152
	v_mfma_f32_16x16x32_bf16 v[92:95], v[230:233], v[124:127], v[92:95]
	v_add_f32_e32 v220, v220, v83
	v_add_f32_e32 v221, v221, v87
	v_mfma_f32_16x16x32_bf16 v[88:91], v[230:233], v[108:111], v[88:91]
	v_cvt_pk_bf16_f32 v218, v72, v73
	ds_read_b128 v[180:183], v209 offset:36864
	v_mfma_f32_16x16x32_bf16 v[60:63], v[234:237], v[204:207], v[60:63]
	v_cvt_pk_bf16_f32 v219, v74, v75
	v_cvt_pk_bf16_f32 v240, v76, v77
	v_mfma_f32_16x16x32_bf16 v[56:59], v[234:237], v[242:245], v[56:59]
	v_cvt_pk_bf16_f32 v241, v78, v79
	ds_read_b128 v[230:233], v246 offset:49152
	s_cmp_eq_u32 s100, 0
	s_cbranch_scc1 .Lattn_pax64
	s_setprio 1
	s_branch .Lattn_pbx64

.Lattn_pbx64:
	s_waitcnt lgkmcnt(6)
	v_mfma_f32_16x16x32_bf16 v[64:67], v[160:163], v[96:99], 0
	v_exp_f32_e32 v88, v88
	v_mfma_f32_16x16x32_bf16 v[68:71], v[160:163], v[112:115], 0
	v_exp_f32_e32 v92, v92
	ds_read_b128 v[234:237], v209 offset:38912
	s_add_u32 s8, s16, 0x3bc00300
	s_addc_u32 s9, s17, 0
	s_add_u32 s6, s15, 0x23a70000
	s_addc_u32 s7, s14, 0
	s_waitcnt lgkmcnt(6)
	v_mfma_f32_16x16x32_bf16 v[0:3], v[164:167], v[216:219], v[0:3]
	v_cvt_pk_bf16_f32 v242, v80, v81
	v_mfma_f32_16x16x32_bf16 v[4:7], v[164:167], v[238:241], v[4:7]
	v_exp_f32_e32 v89, v89
	ds_read_b128 v[160:163], v201 offset:53248
	s_waitcnt vmcnt(4)
	ds_write_b128 v225, v[152:155] offset:16384
	s_waitcnt lgkmcnt(7)
	v_mfma_f32_16x16x32_bf16 v[68:71], v[168:171], v[116:119], v[68:71]
	v_exp_f32_e32 v93, v93
	v_mfma_f32_16x16x32_bf16 v[64:67], v[168:171], v[100:103], v[64:67]
	v_cvt_pk_bf16_f32 v243, v82, v83
	ds_read_b128 v[164:167], v209 offset:40960
	ds_write_b128 v226, v[156:159] offset:16384
	s_waitcnt lgkmcnt(8)
	v_mfma_f32_16x16x32_bf16 v[12:15], v[172:175], v[238:241], v[12:15]
	v_exp_f32_e32 v90, v90
	v_mfma_f32_16x16x32_bf16 v[8:11], v[172:175], v[216:219], v[8:11]
	v_exp_f32_e32 v94, v94
	ds_read_b128 v[168:171], v202 offset:53248
	ds_write_b64 v227, v[132:133] offset:0
	s_waitcnt lgkmcnt(9)
	v_mfma_f32_16x16x32_bf16 v[64:67], v[176:179], v[104:107], v[64:67]
	v_cvt_pk_bf16_f32 v204, v84, v85
	v_mfma_f32_16x16x32_bf16 v[68:71], v[176:179], v[120:123], v[68:71]
	v_exp_f32_e32 v91, v91
	ds_read_b128 v[172:175], v209 offset:43008
	ds_write_b64 v228, v[134:135] offset:0
	s_waitcnt lgkmcnt(10)
	v_mfma_f32_16x16x32_bf16 v[16:19], v[180:183], v[216:219], v[16:19]
	v_exp_f32_e32 v95, v95
	v_mfma_f32_16x16x32_bf16 v[20:23], v[180:183], v[238:241], v[20:23]
	v_cvt_pk_bf16_f32 v205, v86, v87
	v_add_f32_e32 v220, v220, v88
	ds_read_b128 v[176:179], v203 offset:53248
	ds_write_b64 v229, v[128:129] offset:0
	s_waitcnt lgkmcnt(11)
	v_mfma_f32_16x16x32_bf16 v[68:71], v[230:233], v[124:127], v[68:71]
	v_add_f32_e32 v221, v221, v92
	v_add_f32_e32 v220, v220, v89
	v_mfma_f32_16x16x32_bf16 v[64:67], v[230:233], v[108:111], v[64:67]
	v_add_f32_e32 v221, v221, v93
	v_cvt_pk_bf16_f32 v244, v88, v89
	ds_read_b128 v[180:183], v209 offset:45056
	ds_write_b64 v184, v[130:131] offset:0
	s_waitcnt lgkmcnt(12)
	v_mfma_f32_16x16x32_bf16 v[28:31], v[234:237], v[238:241], v[28:31]
	v_cvt_pk_bf16_f32 v245, v90, v91
	v_cvt_pk_bf16_f32 v206, v92, v93
	v_mfma_f32_16x16x32_bf16 v[24:27], v[234:237], v[216:219], v[24:27]
	v_cvt_pk_bf16_f32 v207, v94, v95
	ds_read_b128 v[230:233], v246 offset:53248
	global_load_dwordx4 v[132:135], v198, s[8:9]
	s_waitcnt lgkmcnt(12)
	v_mfma_f32_16x16x32_bf16 v[72:75], v[160:163], v[96:99], 0
	v_add_f32_e32 v220, v220, v90
	v_add_f32_e32 v221, v221, v94
	v_mfma_f32_16x16x32_bf16 v[76:79], v[160:163], v[112:115], 0
	v_add_f32_e32 v220, v220, v91
	v_add_f32_e32 v221, v221, v95
	ds_read_b128 v[234:237], v209 offset:47104
	global_load_dwordx4 v[128:131], v199, s[8:9]
	s_waitcnt lgkmcnt(11)
	v_mfma_f32_16x16x32_bf16 v[32:35], v[164:167], v[216:219], v[32:35]
	v_add_f32_e32 v194, v194, v220
	v_add_f32_e32 v195, v195, v221
	v_mfma_f32_16x16x32_bf16 v[36:39], v[164:167], v[238:241], v[36:39]
	v_exp_f32_e32 v64, v64
	ds_read_b128 v[160:163], v201 offset:57344
	global_load_dwordx4 v[152:155], v196, s[6:7]
	s_waitcnt lgkmcnt(10)
	v_mfma_f32_16x16x32_bf16 v[76:79], v[168:171], v[116:119], v[76:79]
	v_exp_f32_e32 v68, v68
	v_mfma_f32_16x16x32_bf16 v[72:75], v[168:171], v[100:103], v[72:75]
	v_exp_f32_e32 v65, v65
	ds_read_b128 v[164:167], v210 offset:32768
	global_load_dwordx4 v[156:159], v197, s[6:7]
	s_waitcnt lgkmcnt(9)
	v_mfma_f32_16x16x32_bf16 v[44:47], v[172:175], v[238:241], v[44:47]
	v_exp_f32_e32 v69, v69
	v_mfma_f32_16x16x32_bf16 v[40:43], v[172:175], v[216:219], v[40:43]
	v_exp_f32_e32 v66, v66
	ds_read_b128 v[168:171], v202 offset:57344
	s_waitcnt lgkmcnt(8)
	v_mfma_f32_16x16x32_bf16 v[72:75], v[176:179], v[104:107], v[72:75]
	v_exp_f32_e32 v70, v70
	v_mfma_f32_16x16x32_bf16 v[76:79], v[176:179], v[120:123], v[76:79]
	v_exp_f32_e32 v67, v67
	ds_read_b128 v[172:175], v210 offset:34816
	s_waitcnt lgkmcnt(7)
	v_mfma_f32_16x16x32_bf16 v[48:51], v[180:183], v[216:219], v[48:51]
	v_exp_f32_e32 v71, v71
	v_mfma_f32_16x16x32_bf16 v[52:55], v[180:183], v[238:241], v[52:55]
	v_add_f32_e32 v220, v64, v65
	ds_read_b128 v[176:179], v203 offset:57344
	s_waitcnt lgkmcnt(6)
	v_mfma_f32_16x16x32_bf16 v[76:79], v[230:233], v[124:127], v[76:79]
	v_add_f32_e32 v221, v68, v69
	v_mfma_f32_16x16x32_bf16 v[72:75], v[230:233], v[108:111], v[72:75]
	v_add_f32_e32 v220, v220, v66
	ds_read_b128 v[180:183], v210 offset:36864
	s_waitcnt lgkmcnt(6)
	v_mfma_f32_16x16x32_bf16 v[60:63], v[234:237], v[238:241], v[60:63]
	v_add_f32_e32 v221, v221, v70
	v_add_f32_e32 v220, v220, v67
	v_mfma_f32_16x16x32_bf16 v[56:59], v[234:237], v[216:219], v[56:59]
	v_add_f32_e32 v221, v221, v71
	ds_read_b128 v[230:233], v246 offset:57344
	s_waitcnt lgkmcnt(6)
	v_mfma_f32_16x16x32_bf16 v[80:83], v[160:163], v[96:99], 0
	v_exp_f32_e32 v72, v72
	v_mfma_f32_16x16x32_bf16 v[84:87], v[160:163], v[112:115], 0
	v_exp_f32_e32 v76, v76
	ds_read_b128 v[234:237], v210 offset:38912
	s_waitcnt lgkmcnt(6)
	v_mfma_f32_16x16x32_bf16 v[0:3], v[164:167], v[242:245], v[0:3]
	v_exp_f32_e32 v73, v73
	v_mfma_f32_16x16x32_bf16 v[4:7], v[164:167], v[204:207], v[4:7]
	v_exp_f32_e32 v77, v77
	ds_read_b128 v[160:163], v201 offset:61440
	s_waitcnt lgkmcnt(6)
	v_mfma_f32_16x16x32_bf16 v[84:87], v[168:171], v[116:119], v[84:87]
	v_exp_f32_e32 v74, v74
	v_mfma_f32_16x16x32_bf16 v[80:83], v[168:171], v[100:103], v[80:83]
	v_exp_f32_e32 v78, v78
	ds_read_b128 v[164:167], v210 offset:40960
	s_waitcnt lgkmcnt(6)
	v_mfma_f32_16x16x32_bf16 v[12:15], v[172:175], v[204:207], v[12:15]
	v_exp_f32_e32 v75, v75
	v_mfma_f32_16x16x32_bf16 v[8:11], v[172:175], v[242:245], v[8:11]
	v_exp_f32_e32 v79, v79
	ds_read_b128 v[168:171], v202 offset:61440
	s_waitcnt lgkmcnt(6)
	v_mfma_f32_16x16x32_bf16 v[80:83], v[176:179], v[104:107], v[80:83]
	v_add_f32_e32 v220, v220, v72
	v_add_f32_e32 v221, v221, v76
	v_mfma_f32_16x16x32_bf16 v[84:87], v[176:179], v[120:123], v[84:87]
	v_add_f32_e32 v220, v220, v73
	ds_read_b128 v[172:175], v210 offset:43008
	s_waitcnt lgkmcnt(6)
	v_mfma_f32_16x16x32_bf16 v[16:19], v[180:183], v[242:245], v[16:19]
	v_add_f32_e32 v221, v221, v77
	v_add_f32_e32 v220, v220, v74
	v_mfma_f32_16x16x32_bf16 v[20:23], v[180:183], v[204:207], v[20:23]
	v_add_f32_e32 v221, v221, v78
	ds_read_b128 v[176:179], v203 offset:61440
	s_waitcnt lgkmcnt(6)
	v_mfma_f32_16x16x32_bf16 v[84:87], v[230:233], v[124:127], v[84:87]
	v_add_f32_e32 v220, v220, v75
	v_add_f32_e32 v221, v221, v79
	v_mfma_f32_16x16x32_bf16 v[80:83], v[230:233], v[108:111], v[80:83]
	v_cvt_pk_bf16_f32 v216, v64, v65
	ds_read_b128 v[180:183], v210 offset:45056
	s_waitcnt lgkmcnt(6)
	v_mfma_f32_16x16x32_bf16 v[28:31], v[234:237], v[204:207], v[28:31]
	v_cvt_pk_bf16_f32 v217, v66, v67
	v_cvt_pk_bf16_f32 v238, v68, v69
	v_mfma_f32_16x16x32_bf16 v[24:27], v[234:237], v[242:245], v[24:27]
	v_cvt_pk_bf16_f32 v239, v70, v71
	ds_read_b128 v[230:233], v246 offset:61440
	s_waitcnt lgkmcnt(6)
	v_mfma_f32_16x16x32_bf16 v[88:91], v[160:163], v[96:99], 0
	v_exp_f32_e32 v80, v80
	v_mfma_f32_16x16x32_bf16 v[92:95], v[160:163], v[112:115], 0
	v_exp_f32_e32 v84, v84
	ds_read_b128 v[234:237], v210 offset:47104
	s_waitcnt lgkmcnt(6)
	v_mfma_f32_16x16x32_bf16 v[32:35], v[164:167], v[242:245], v[32:35]
	v_exp_f32_e32 v81, v81
	v_mfma_f32_16x16x32_bf16 v[36:39], v[164:167], v[204:207], v[36:39]
	v_exp_f32_e32 v85, v85
	ds_read_b128 v[160:163], v201 offset:0
	s_waitcnt lgkmcnt(6)
	v_mfma_f32_16x16x32_bf16 v[92:95], v[168:171], v[116:119], v[92:95]
	v_exp_f32_e32 v82, v82
	v_mfma_f32_16x16x32_bf16 v[88:91], v[168:171], v[100:103], v[88:91]
	v_exp_f32_e32 v86, v86
	ds_read_b128 v[164:167], v209 offset:49152
	s_waitcnt lgkmcnt(6)
	v_mfma_f32_16x16x32_bf16 v[44:47], v[172:175], v[204:207], v[44:47]
	v_exp_f32_e32 v83, v83
	v_mfma_f32_16x16x32_bf16 v[40:43], v[172:175], v[242:245], v[40:43]
	v_exp_f32_e32 v87, v87
	ds_read_b128 v[168:171], v202 offset:0
	s_waitcnt lgkmcnt(6)
	v_mfma_f32_16x16x32_bf16 v[88:91], v[176:179], v[104:107], v[88:91]
	v_add_f32_e32 v220, v220, v80
	v_add_f32_e32 v221, v221, v84
	v_mfma_f32_16x16x32_bf16 v[92:95], v[176:179], v[120:123], v[92:95]
	v_add_f32_e32 v220, v220, v81
	ds_read_b128 v[172:175], v209 offset:51200
	s_waitcnt lgkmcnt(6)
	v_mfma_f32_16x16x32_bf16 v[48:51], v[180:183], v[242:245], v[48:51]
	v_add_f32_e32 v221, v221, v85
	v_add_f32_e32 v220, v220, v82
	v_mfma_f32_16x16x32_bf16 v[52:55], v[180:183], v[204:207], v[52:55]
	v_add_f32_e32 v221, v221, v86
	ds_read_b128 v[176:179], v203 offset:0
	s_waitcnt lgkmcnt(6)
	v_mfma_f32_16x16x32_bf16 v[92:95], v[230:233], v[124:127], v[92:95]
	v_add_f32_e32 v220, v220, v83
	v_add_f32_e32 v221, v221, v87
	v_mfma_f32_16x16x32_bf16 v[88:91], v[230:233], v[108:111], v[88:91]
	v_cvt_pk_bf16_f32 v218, v72, v73
	ds_read_b128 v[180:183], v209 offset:53248
	s_waitcnt lgkmcnt(6)
	v_mfma_f32_16x16x32_bf16 v[60:63], v[234:237], v[204:207], v[60:63]
	v_cvt_pk_bf16_f32 v219, v74, v75
	v_cvt_pk_bf16_f32 v240, v76, v77
	v_mfma_f32_16x16x32_bf16 v[56:59], v[234:237], v[242:245], v[56:59]
	v_cvt_pk_bf16_f32 v241, v78, v79
	ds_read_b128 v[230:233], v246 offset:0
	s_waitcnt lgkmcnt(6)
	v_mfma_f32_16x16x32_bf16 v[64:67], v[160:163], v[96:99], 0
	v_exp_f32_e32 v88, v88
	v_mfma_f32_16x16x32_bf16 v[68:71], v[160:163], v[112:115], 0
	v_exp_f32_e32 v92, v92
	ds_read_b128 v[234:237], v209 offset:55296
	s_add_u32 s8, s16, 0x3bc00380
	s_addc_u32 s9, s17, 0
	s_add_u32 s6, s15, 0x23a80000
	s_addc_u32 s7, s14, 0
	s_waitcnt lgkmcnt(6)
	v_mfma_f32_16x16x32_bf16 v[0:3], v[164:167], v[216:219], v[0:3]
	v_cvt_pk_bf16_f32 v242, v80, v81
	v_mfma_f32_16x16x32_bf16 v[4:7], v[164:167], v[238:241], v[4:7]
	v_exp_f32_e32 v89, v89
	ds_read_b128 v[160:163], v201 offset:4096
	s_waitcnt vmcnt(4)
	ds_write_b128 v225, v[136:139] offset:32768
	s_waitcnt lgkmcnt(7)
	v_mfma_f32_16x16x32_bf16 v[68:71], v[168:171], v[116:119], v[68:71]
	v_exp_f32_e32 v93, v93
	v_mfma_f32_16x16x32_bf16 v[64:67], v[168:171], v[100:103], v[64:67]
	v_cvt_pk_bf16_f32 v243, v82, v83
	ds_read_b128 v[164:167], v209 offset:57344
	ds_write_b128 v226, v[140:143] offset:32768
	s_waitcnt lgkmcnt(8)
	v_mfma_f32_16x16x32_bf16 v[12:15], v[172:175], v[238:241], v[12:15]
	v_exp_f32_e32 v90, v90
	v_mfma_f32_16x16x32_bf16 v[8:11], v[172:175], v[216:219], v[8:11]
	v_exp_f32_e32 v94, v94
	ds_read_b128 v[168:171], v202 offset:4096
	ds_write_b64 v227, v[148:149] offset:16384
	s_waitcnt lgkmcnt(9)
	v_mfma_f32_16x16x32_bf16 v[64:67], v[176:179], v[104:107], v[64:67]
	v_cvt_pk_bf16_f32 v204, v84, v85
	v_mfma_f32_16x16x32_bf16 v[68:71], v[176:179], v[120:123], v[68:71]
	v_exp_f32_e32 v91, v91
	ds_read_b128 v[172:175], v209 offset:59392
	ds_write_b64 v228, v[150:151] offset:16384
	s_waitcnt lgkmcnt(10)
	v_mfma_f32_16x16x32_bf16 v[16:19], v[180:183], v[216:219], v[16:19]
	v_exp_f32_e32 v95, v95
	v_mfma_f32_16x16x32_bf16 v[20:23], v[180:183], v[238:241], v[20:23]
	v_cvt_pk_bf16_f32 v205, v86, v87
	v_add_f32_e32 v220, v220, v88
	ds_read_b128 v[176:179], v203 offset:4096
	ds_write_b64 v229, v[144:145] offset:16384
	s_waitcnt lgkmcnt(11)
	v_mfma_f32_16x16x32_bf16 v[68:71], v[230:233], v[124:127], v[68:71]
	v_add_f32_e32 v221, v221, v92
	v_add_f32_e32 v220, v220, v89
	v_mfma_f32_16x16x32_bf16 v[64:67], v[230:233], v[108:111], v[64:67]
	v_add_f32_e32 v221, v221, v93
	v_cvt_pk_bf16_f32 v244, v88, v89
	ds_read_b128 v[180:183], v209 offset:61440
	ds_write_b64 v184, v[146:147] offset:16384
	s_waitcnt lgkmcnt(12)
	v_mfma_f32_16x16x32_bf16 v[28:31], v[234:237], v[238:241], v[28:31]
	v_cvt_pk_bf16_f32 v245, v90, v91
	v_cvt_pk_bf16_f32 v206, v92, v93
	v_mfma_f32_16x16x32_bf16 v[24:27], v[234:237], v[216:219], v[24:27]
	v_cvt_pk_bf16_f32 v207, v94, v95
	ds_read_b128 v[230:233], v246 offset:4096
	global_load_dwordx4 v[148:151], v198, s[8:9]
	s_cmp_eq_u32 s100, 1
	s_cbranch_scc1 .Lattn_pax104
	s_setprio 1
	s_branch .Lattn_pbx104

.Lattn_pbx104:
	s_waitcnt lgkmcnt(12)
	v_mfma_f32_16x16x32_bf16 v[72:75], v[160:163], v[96:99], 0
	v_add_f32_e32 v220, v220, v90
	v_add_f32_e32 v221, v221, v94
	v_mfma_f32_16x16x32_bf16 v[76:79], v[160:163], v[112:115], 0
	v_add_f32_e32 v220, v220, v91
	v_add_f32_e32 v221, v221, v95
	ds_read_b128 v[234:237], v209 offset:63488
	global_load_dwordx4 v[144:147], v199, s[8:9]
	s_waitcnt lgkmcnt(11)
	v_mfma_f32_16x16x32_bf16 v[32:35], v[164:167], v[216:219], v[32:35]
	v_add_f32_e32 v194, v194, v220
	v_add_f32_e32 v195, v195, v221
	v_mfma_f32_16x16x32_bf16 v[36:39], v[164:167], v[238:241], v[36:39]
	v_exp_f32_e32 v64, v64
	ds_read_b128 v[160:163], v201 offset:8192
	global_load_dwordx4 v[136:139], v196, s[6:7]
	s_waitcnt lgkmcnt(10)
	v_mfma_f32_16x16x32_bf16 v[76:79], v[168:171], v[116:119], v[76:79]
	v_exp_f32_e32 v68, v68
	v_mfma_f32_16x16x32_bf16 v[72:75], v[168:171], v[100:103], v[72:75]
	v_exp_f32_e32 v65, v65
	ds_read_b128 v[164:167], v210 offset:49152
	global_load_dwordx4 v[140:143], v197, s[6:7]
	s_waitcnt lgkmcnt(9)
	v_mfma_f32_16x16x32_bf16 v[44:47], v[172:175], v[238:241], v[44:47]
	v_exp_f32_e32 v69, v69
	v_mfma_f32_16x16x32_bf16 v[40:43], v[172:175], v[216:219], v[40:43]
	v_exp_f32_e32 v66, v66
	ds_read_b128 v[168:171], v202 offset:8192
	s_waitcnt lgkmcnt(8)
	v_mfma_f32_16x16x32_bf16 v[72:75], v[176:179], v[104:107], v[72:75]
	v_exp_f32_e32 v70, v70
	v_mfma_f32_16x16x32_bf16 v[76:79], v[176:179], v[120:123], v[76:79]
	v_exp_f32_e32 v67, v67
	ds_read_b128 v[172:175], v210 offset:51200
	s_waitcnt lgkmcnt(7)
	v_mfma_f32_16x16x32_bf16 v[48:51], v[180:183], v[216:219], v[48:51]
	v_exp_f32_e32 v71, v71
	v_mfma_f32_16x16x32_bf16 v[52:55], v[180:183], v[238:241], v[52:55]
	v_add_f32_e32 v220, v64, v65
	ds_read_b128 v[176:179], v203 offset:8192
	s_waitcnt lgkmcnt(6)
	v_mfma_f32_16x16x32_bf16 v[76:79], v[230:233], v[124:127], v[76:79]
	v_add_f32_e32 v221, v68, v69
	v_mfma_f32_16x16x32_bf16 v[72:75], v[230:233], v[108:111], v[72:75]
	v_add_f32_e32 v220, v220, v66
	ds_read_b128 v[180:183], v210 offset:53248
	s_waitcnt lgkmcnt(6)
	v_mfma_f32_16x16x32_bf16 v[60:63], v[234:237], v[238:241], v[60:63]
	v_add_f32_e32 v221, v221, v70
	v_add_f32_e32 v220, v220, v67
	v_mfma_f32_16x16x32_bf16 v[56:59], v[234:237], v[216:219], v[56:59]
	v_add_f32_e32 v221, v221, v71
	ds_read_b128 v[230:233], v246 offset:8192
	s_waitcnt lgkmcnt(6)
	v_mfma_f32_16x16x32_bf16 v[80:83], v[160:163], v[96:99], 0
	v_exp_f32_e32 v72, v72
	v_mfma_f32_16x16x32_bf16 v[84:87], v[160:163], v[112:115], 0
	v_exp_f32_e32 v76, v76
	ds_read_b128 v[234:237], v210 offset:55296
	s_waitcnt lgkmcnt(6)
	v_mfma_f32_16x16x32_bf16 v[0:3], v[164:167], v[242:245], v[0:3]
	v_exp_f32_e32 v73, v73
	v_mfma_f32_16x16x32_bf16 v[4:7], v[164:167], v[204:207], v[4:7]
	v_exp_f32_e32 v77, v77
	ds_read_b128 v[160:163], v201 offset:12288
	s_waitcnt lgkmcnt(6)
	v_mfma_f32_16x16x32_bf16 v[84:87], v[168:171], v[116:119], v[84:87]
	v_exp_f32_e32 v74, v74
	v_mfma_f32_16x16x32_bf16 v[80:83], v[168:171], v[100:103], v[80:83]
	v_exp_f32_e32 v78, v78
	ds_read_b128 v[164:167], v210 offset:57344
	s_waitcnt lgkmcnt(6)
	v_mfma_f32_16x16x32_bf16 v[12:15], v[172:175], v[204:207], v[12:15]
	v_exp_f32_e32 v75, v75
	v_mfma_f32_16x16x32_bf16 v[8:11], v[172:175], v[242:245], v[8:11]
	v_exp_f32_e32 v79, v79
	ds_read_b128 v[168:171], v202 offset:12288
	s_waitcnt lgkmcnt(6)
	v_mfma_f32_16x16x32_bf16 v[80:83], v[176:179], v[104:107], v[80:83]
	v_add_f32_e32 v220, v220, v72
	v_add_f32_e32 v221, v221, v76
	v_mfma_f32_16x16x32_bf16 v[84:87], v[176:179], v[120:123], v[84:87]
	v_add_f32_e32 v220, v220, v73
	ds_read_b128 v[172:175], v210 offset:59392
	s_add_u32 s10, s10, 0x200
	s_addc_u32 s11, s11, 0
	s_add_u32 s12, s12, 0x40000
	s_addc_u32 s13, s13, 0
	s_add_i32 s4, s4, 4
	s_cmpk_lt_u32 s4, 0x104
	s_cselect_b64 s[6:7], -1, 0
	s_and_b64 s[6:7], s[0:1], s[6:7]
	s_and_b64 vcc, exec, s[6:7]
	s_waitcnt lgkmcnt(6)
	v_mfma_f32_16x16x32_bf16 v[16:19], v[180:183], v[242:245], v[16:19]
	v_add_f32_e32 v221, v221, v77
	v_add_f32_e32 v220, v220, v74
	v_mfma_f32_16x16x32_bf16 v[20:23], v[180:183], v[204:207], v[20:23]
	v_add_f32_e32 v221, v221, v78
	ds_read_b128 v[176:179], v203 offset:12288
	s_waitcnt lgkmcnt(6)
	v_mfma_f32_16x16x32_bf16 v[84:87], v[230:233], v[124:127], v[84:87]
	v_add_f32_e32 v220, v220, v75
	v_add_f32_e32 v221, v221, v79
	v_mfma_f32_16x16x32_bf16 v[80:83], v[230:233], v[108:111], v[80:83]
	v_cvt_pk_bf16_f32 v216, v64, v65
	ds_read_b128 v[180:183], v210 offset:61440
	s_waitcnt lgkmcnt(6)
	v_mfma_f32_16x16x32_bf16 v[28:31], v[234:237], v[204:207], v[28:31]
	v_cvt_pk_bf16_f32 v217, v66, v67
	v_cvt_pk_bf16_f32 v238, v68, v69
	v_mfma_f32_16x16x32_bf16 v[24:27], v[234:237], v[242:245], v[24:27]
	v_cvt_pk_bf16_f32 v239, v70, v71
	ds_read_b128 v[230:233], v246 offset:12288
	s_waitcnt lgkmcnt(6)
	v_mfma_f32_16x16x32_bf16 v[88:91], v[160:163], v[96:99], 0
	v_exp_f32_e32 v80, v80
	v_mfma_f32_16x16x32_bf16 v[92:95], v[160:163], v[112:115], 0
	v_exp_f32_e32 v84, v84
	ds_read_b128 v[234:237], v210 offset:63488
	s_waitcnt lgkmcnt(6)
	v_mfma_f32_16x16x32_bf16 v[32:35], v[164:167], v[242:245], v[32:35]
	v_exp_f32_e32 v81, v81
	v_mfma_f32_16x16x32_bf16 v[36:39], v[164:167], v[204:207], v[36:39]
	v_exp_f32_e32 v85, v85
	s_waitcnt lgkmcnt(5)
	v_mfma_f32_16x16x32_bf16 v[92:95], v[168:171], v[116:119], v[92:95]
	v_exp_f32_e32 v82, v82
	v_mfma_f32_16x16x32_bf16 v[88:91], v[168:171], v[100:103], v[88:91]
	v_exp_f32_e32 v86, v86
	s_waitcnt lgkmcnt(4)
	v_mfma_f32_16x16x32_bf16 v[44:47], v[172:175], v[204:207], v[44:47]
	v_exp_f32_e32 v83, v83
	v_mfma_f32_16x16x32_bf16 v[40:43], v[172:175], v[242:245], v[40:43]
	v_exp_f32_e32 v87, v87
	s_waitcnt lgkmcnt(3)
	v_mfma_f32_16x16x32_bf16 v[88:91], v[176:179], v[104:107], v[88:91]
	v_add_f32_e32 v220, v220, v80
	v_add_f32_e32 v221, v221, v84
	v_mfma_f32_16x16x32_bf16 v[92:95], v[176:179], v[120:123], v[92:95]
	v_add_f32_e32 v220, v220, v81
	s_waitcnt lgkmcnt(0)
	s_barrier
	ds_read_b128 v[160:163], v201 offset:16384
	ds_read_b128 v[164:167], v209 offset:0
	ds_read_b128 v[168:171], v202 offset:16384
	ds_read_b128 v[172:175], v209 offset:2048
	v_mfma_f32_16x16x32_bf16 v[48:51], v[180:183], v[242:245], v[48:51]
	v_add_f32_e32 v221, v221, v85
	v_add_f32_e32 v220, v220, v82
	v_mfma_f32_16x16x32_bf16 v[52:55], v[180:183], v[204:207], v[52:55]
	v_add_f32_e32 v221, v221, v86
	ds_read_b128 v[176:179], v203 offset:16384
	v_mfma_f32_16x16x32_bf16 v[92:95], v[230:233], v[124:127], v[92:95]
	v_add_f32_e32 v220, v220, v83
	v_add_f32_e32 v221, v221, v87
	v_mfma_f32_16x16x32_bf16 v[88:91], v[230:233], v[108:111], v[88:91]
	v_cvt_pk_bf16_f32 v218, v72, v73
	ds_read_b128 v[180:183], v209 offset:4096
	v_mfma_f32_16x16x32_bf16 v[60:63], v[234:237], v[204:207], v[60:63]
	v_cvt_pk_bf16_f32 v219, v74, v75
	v_cvt_pk_bf16_f32 v240, v76, v77
	v_mfma_f32_16x16x32_bf16 v[56:59], v[234:237], v[242:245], v[56:59]
	v_cvt_pk_bf16_f32 v241, v78, v79
	ds_read_b128 v[230:233], v246 offset:16384
	s_cbranch_vccnz .LBB0_734
	s_setprio 0
	s_waitcnt vmcnt(0)
	s_nop 7
	s_nop 7
	ds_swizzle_b32 v64, v194 offset:swizzle(SWAP,16)
	s_waitcnt lgkmcnt(0)
	v_add_f32_e32 v194, v194, v64
	v_mov_b32_e32 v65, v194
	s_nop 1
	v_permlane32_swap_b32_e32 v194, v65
	v_add_f32_e32 v194, v194, v65
	s_nop 0
	v_rcp_f32_e32 v66, v194
	ds_swizzle_b32 v64, v195 offset:swizzle(SWAP,16)
	s_waitcnt lgkmcnt(0)
	v_add_f32_e32 v195, v195, v64
	v_mov_b32_e32 v65, v195
	s_nop 1
	v_permlane32_swap_b32_e32 v195, v65
	v_add_f32_e32 v195, v195, v65
	s_nop 0
	v_rcp_f32_e32 v67, v195
	v_readlane_b32 s100, v250, 8
	v_mbcnt_lo_u32_b32 v68, -1, 0
	v_mbcnt_hi_u32_b32 v68, -1, v68
	v_and_b32_e32 v69, 15, v68
	v_lshrrev_b32_e32 v70, 4, v68
	s_lshr_b32 s101, s100, 1
	v_add_u32_e32 v69, s101, v69
	v_lshlrev_b32_e32 v69, 12, v69
	v_and_b32_e32 v71, 1, v70
	v_lshlrev_b32_e32 v71, 5, v71
	v_and_b32_e32 v70, 2, v70
	v_lshl_add_u32 v71, v70, 3, v71
	v_add_u32_e32 v70, v69, v71
	v_add_u32_e32 v71, 0x10000, v70
	v_mul_f32_e32 v0, v0, v66
	v_mul_f32_e32 v1, v1, v66
	v_mul_f32_e32 v2, v2, v66
	v_mul_f32_e32 v3, v3, v66
	v_mul_f32_e32 v8, v8, v66
	v_mul_f32_e32 v9, v9, v66
	v_mul_f32_e32 v10, v10, v66
	v_mul_f32_e32 v11, v11, v66
	v_cvt_pk_bf16_f32 v72, v0, v1
	v_cvt_pk_bf16_f32 v73, v2, v3
	v_cvt_pk_bf16_f32 v74, v8, v9
	v_cvt_pk_bf16_f32 v75, v10, v11
	s_nop 1
	v_permlane16_swap_b32_e32 v72, v74
	v_permlane16_swap_b32_e32 v73, v75
	s_nop 1
	global_store_dwordx4 v70, v[72:75], s[58:59] offset:0
	v_mul_f32_e32 v16, v16, v66
	v_mul_f32_e32 v17, v17, v66
	v_mul_f32_e32 v18, v18, v66
	v_mul_f32_e32 v19, v19, v66
	v_mul_f32_e32 v24, v24, v66
	v_mul_f32_e32 v25, v25, v66
	v_mul_f32_e32 v26, v26, v66
	v_mul_f32_e32 v27, v27, v66
	v_cvt_pk_bf16_f32 v76, v16, v17
	v_cvt_pk_bf16_f32 v77, v18, v19
	v_cvt_pk_bf16_f32 v78, v24, v25
	v_cvt_pk_bf16_f32 v79, v26, v27
	s_nop 1
	v_permlane16_swap_b32_e32 v76, v78
	v_permlane16_swap_b32_e32 v77, v79
	s_nop 1
	global_store_dwordx4 v70, v[76:79], s[58:59] offset:64
	v_mul_f32_e32 v32, v32, v66
	v_mul_f32_e32 v33, v33, v66
	v_mul_f32_e32 v34, v34, v66
	v_mul_f32_e32 v35, v35, v66
	v_mul_f32_e32 v40, v40, v66
	v_mul_f32_e32 v41, v41, v66
	v_mul_f32_e32 v42, v42, v66
	v_mul_f32_e32 v43, v43, v66
	v_cvt_pk_bf16_f32 v80, v32, v33
	v_cvt_pk_bf16_f32 v81, v34, v35
	v_cvt_pk_bf16_f32 v82, v40, v41
	v_cvt_pk_bf16_f32 v83, v42, v43
	s_nop 1
	v_permlane16_swap_b32_e32 v80, v82
	v_permlane16_swap_b32_e32 v81, v83
	s_nop 1
	global_store_dwordx4 v70, v[80:83], s[58:59] offset:128
	v_mul_f32_e32 v48, v48, v66
	v_mul_f32_e32 v49, v49, v66
	v_mul_f32_e32 v50, v50, v66
	v_mul_f32_e32 v51, v51, v66
	v_mul_f32_e32 v56, v56, v66
	v_mul_f32_e32 v57, v57, v66
	v_mul_f32_e32 v58, v58, v66
	v_mul_f32_e32 v59, v59, v66
	v_cvt_pk_bf16_f32 v84, v48, v49
	v_cvt_pk_bf16_f32 v85, v50, v51
	v_cvt_pk_bf16_f32 v86, v56, v57
	v_cvt_pk_bf16_f32 v87, v58, v59
	s_nop 1
	v_permlane16_swap_b32_e32 v84, v86
	v_permlane16_swap_b32_e32 v85, v87
	s_nop 1
	global_store_dwordx4 v70, v[84:87], s[58:59] offset:192
	v_mul_f32_e32 v4, v4, v67
	v_mul_f32_e32 v5, v5, v67
	v_mul_f32_e32 v6, v6, v67
	v_mul_f32_e32 v7, v7, v67
	v_mul_f32_e32 v12, v12, v67
	v_mul_f32_e32 v13, v13, v67
	v_mul_f32_e32 v14, v14, v67
	v_mul_f32_e32 v15, v15, v67
	v_cvt_pk_bf16_f32 v88, v4, v5
	v_cvt_pk_bf16_f32 v89, v6, v7
	v_cvt_pk_bf16_f32 v90, v12, v13
	v_cvt_pk_bf16_f32 v91, v14, v15
	s_nop 1
	v_permlane16_swap_b32_e32 v88, v90
	v_permlane16_swap_b32_e32 v89, v91
	s_nop 1
	global_store_dwordx4 v71, v[88:91], s[58:59] offset:0
	v_mul_f32_e32 v20, v20, v67
	v_mul_f32_e32 v21, v21, v67
	v_mul_f32_e32 v22, v22, v67
	v_mul_f32_e32 v23, v23, v67
	v_mul_f32_e32 v28, v28, v67
	v_mul_f32_e32 v29, v29, v67
	v_mul_f32_e32 v30, v30, v67
	v_mul_f32_e32 v31, v31, v67
	v_cvt_pk_bf16_f32 v92, v20, v21
	v_cvt_pk_bf16_f32 v93, v22, v23
	v_cvt_pk_bf16_f32 v94, v28, v29
	v_cvt_pk_bf16_f32 v95, v30, v31
	s_nop 1
	v_permlane16_swap_b32_e32 v92, v94
	v_permlane16_swap_b32_e32 v93, v95
	s_nop 1
	global_store_dwordx4 v71, v[92:95], s[58:59] offset:64
	v_mul_f32_e32 v36, v36, v67
	v_mul_f32_e32 v37, v37, v67
	v_mul_f32_e32 v38, v38, v67
	v_mul_f32_e32 v39, v39, v67
	v_mul_f32_e32 v44, v44, v67
	v_mul_f32_e32 v45, v45, v67
	v_mul_f32_e32 v46, v46, v67
	v_mul_f32_e32 v47, v47, v67
	v_cvt_pk_bf16_f32 v72, v36, v37
	v_cvt_pk_bf16_f32 v73, v38, v39
	v_cvt_pk_bf16_f32 v74, v44, v45
	v_cvt_pk_bf16_f32 v75, v46, v47
	s_nop 1
	v_permlane16_swap_b32_e32 v72, v74
	v_permlane16_swap_b32_e32 v73, v75
	s_nop 1
	global_store_dwordx4 v71, v[72:75], s[58:59] offset:128
	v_mul_f32_e32 v52, v52, v67
	v_mul_f32_e32 v53, v53, v67
	v_mul_f32_e32 v54, v54, v67
	v_mul_f32_e32 v55, v55, v67
	v_mul_f32_e32 v60, v60, v67
	v_mul_f32_e32 v61, v61, v67
	v_mul_f32_e32 v62, v62, v67
	v_mul_f32_e32 v63, v63, v67
	v_cvt_pk_bf16_f32 v76, v52, v53
	v_cvt_pk_bf16_f32 v77, v54, v55
	v_cvt_pk_bf16_f32 v78, v60, v61
	v_cvt_pk_bf16_f32 v79, v62, v63
	s_nop 1
	v_permlane16_swap_b32_e32 v76, v78
	v_permlane16_swap_b32_e32 v77, v79
	s_nop 1
	global_store_dwordx4 v71, v[76:79], s[58:59] offset:192
	s_barrier
